# w1f8
# speedup vs baseline: 1.1078x; 1.1065x over previous
.LBB0_68:
	s_andn2_saveexec_b64 s[0:1], s[2:3]
	s_cbranch_execz .LBB0_359
	v_lshrrev_b32_e32 v1, 6, v7
	v_and_b32_e32 v2, 31, v0
	v_bfe_u32 v3, v0, 5, 1
	v_lshlrev_b32_e32 v5, 4, v7
	v_readfirstlane_b32 s10, v1
	v_cmp_ne_u32_e32 vcc, 0, v3
	s_and_b32 s11, s10, 1
	s_bfe_u32 s12, s10, 0x20001
	s_lshr_b32 s13, s10, 3
	s_lshl_b32 s13, s13, 2
	s_lshl1_add_u32 s16, s11, s13
	s_add_u32 s17, s16, 1
	s_lshl_b32 s12, s12, 7
	v_lshl_add_u32 v4, v2, 2, s12
	s_waitcnt lgkmcnt(0)
	s_lshl2_add_u32 s20, s16, 0x16
	s_mov_b32 s21, 0xa800
	s_mov_b32 s22, 0x41800000
	s_mov_b32 s23, 0x41800000
	s_cmp_eq_u32 s16, 0
	s_cselect_b32 s20, 0x0, s20
	s_cselect_b32 s21, 0x1c00, s21
	s_cmp_eq_u32 s16, 22
	s_cselect_b32 s22, 0, s22
	s_cselect_b32 s23, 0, s23
	s_lshl_b32 s20, s20, 9
	v_mad_u32_u24 v6, v3, s21, v4
	v_add_u32_e32 v6, s20, v6
	v_mov_b32_e32 v32, s22
	v_mov_b32_e32 v8, s23
	global_load_dword v16, v6, s[8:9]
	v_cndmask_b32_e32 v32, v32, v8, vcc
	s_lshl2_add_u32 s20, s16, 0xb8
	s_mov_b32 s21, 0xa800
	s_mov_b32 s22, 0x41000000
	s_mov_b32 s23, 0x41000000
	s_cmp_eq_u32 s16, 0
	s_cselect_b32 s20, 0x1, s20
	s_cselect_b32 s21, 0x1c00, s21
	s_cselect_b32 s22, 0x41800000, s22
	s_cselect_b32 s23, 0x41800000, s23
	s_cmp_eq_u32 s16, 22
	s_cselect_b32 s22, 0, s22
	s_cselect_b32 s23, 0, s23
	s_lshl_b32 s20, s20, 9
	v_mad_u32_u24 v6, v3, s21, v4
	v_add_u32_e32 v6, s20, v6
	v_mov_b32_e32 v33, s22
	v_mov_b32_e32 v8, s23
	global_load_dword v17, v6, s[8:9]
	v_cndmask_b32_e32 v33, v33, v8, vcc
	s_lshl2_add_u32 s20, s16, 0x17
	s_mov_b32 s21, 0xa800
	s_mov_b32 s22, 0x41800000
	s_mov_b32 s23, 0x41800000
	s_cmp_eq_u32 s16, 0
	s_cselect_b32 s20, 0x2, s20
	s_cselect_b32 s21, 0x1c00, s21
	s_cmp_eq_u32 s16, 22
	s_cselect_b32 s22, 0, s22
	s_cselect_b32 s23, 0, s23
	s_lshl_b32 s20, s20, 9
	v_mad_u32_u24 v6, v3, s21, v4
	v_add_u32_e32 v6, s20, v6
	v_mov_b32_e32 v34, s22
	v_mov_b32_e32 v8, s23
	global_load_dword v18, v6, s[8:9]
	v_cndmask_b32_e32 v34, v34, v8, vcc
	s_lshl2_add_u32 s20, s16, 0xb9
	s_mov_b32 s21, 0xa800
	s_mov_b32 s22, 0x41000000
	s_mov_b32 s23, 0x41000000
	s_cmp_eq_u32 s16, 0
	s_cselect_b32 s20, 0x3, s20
	s_cselect_b32 s21, 0x1c00, s21
	s_cselect_b32 s22, 0x41800000, s22
	s_cselect_b32 s23, 0x41800000, s23
	s_cmp_eq_u32 s16, 22
	s_cselect_b32 s22, 0, s22
	s_cselect_b32 s23, 0, s23
	s_lshl_b32 s20, s20, 9
	v_mad_u32_u24 v6, v3, s21, v4
	v_add_u32_e32 v6, s20, v6
	v_mov_b32_e32 v35, s22
	v_mov_b32_e32 v8, s23
	global_load_dword v19, v6, s[8:9]
	v_cndmask_b32_e32 v35, v35, v8, vcc
	s_lshl2_add_u32 s20, s16, 0x18
	s_mov_b32 s21, 0xa800
	s_mov_b32 s22, 0x41800000
	s_mov_b32 s23, 0x41800000
	s_cmp_eq_u32 s16, 0
	s_cselect_b32 s20, 0x4, s20
	s_cselect_b32 s21, 0x1c00, s21
	s_cmp_eq_u32 s16, 22
	s_cselect_b32 s22, 0, s22
	s_cselect_b32 s23, 0, s23
	s_lshl_b32 s20, s20, 9
	v_mad_u32_u24 v6, v3, s21, v4
	v_add_u32_e32 v6, s20, v6
	v_mov_b32_e32 v36, s22
	v_mov_b32_e32 v8, s23
	global_load_dword v20, v6, s[8:9]
	v_cndmask_b32_e32 v36, v36, v8, vcc
	s_lshl2_add_u32 s20, s16, 0xba
	s_mov_b32 s21, 0xa800
	s_mov_b32 s22, 0x41000000
	s_mov_b32 s23, 0x41000000
	s_cmp_eq_u32 s16, 0
	s_cselect_b32 s20, 0x5, s20
	s_cselect_b32 s21, 0x1c00, s21
	s_cselect_b32 s22, 0x41800000, s22
	s_cselect_b32 s23, 0x41800000, s23
	s_cmp_eq_u32 s16, 22
	s_cselect_b32 s22, 0, s22
	s_cselect_b32 s23, 0, s23
	s_lshl_b32 s20, s20, 9
	v_mad_u32_u24 v6, v3, s21, v4
	v_add_u32_e32 v6, s20, v6
	v_mov_b32_e32 v37, s22
	v_mov_b32_e32 v8, s23
	global_load_dword v21, v6, s[8:9]
	v_cndmask_b32_e32 v37, v37, v8, vcc
	s_lshl2_add_u32 s20, s16, 0x19
	s_mov_b32 s21, 0xa800
	s_mov_b32 s22, 0x41800000
	s_mov_b32 s23, 0x41800000
	s_cmp_eq_u32 s16, 0
	s_cselect_b32 s20, 0x6, s20
	s_cselect_b32 s21, 0x1c00, s21
	s_cmp_eq_u32 s16, 22
	s_cselect_b32 s22, 0, s22
	s_cselect_b32 s23, 0, s23
	s_lshl_b32 s20, s20, 9
	v_mad_u32_u24 v6, v3, s21, v4
	v_add_u32_e32 v6, s20, v6
	v_mov_b32_e32 v38, s22
	v_mov_b32_e32 v8, s23
	global_load_dword v22, v6, s[8:9]
	v_cndmask_b32_e32 v38, v38, v8, vcc
	s_lshl2_add_u32 s20, s16, 0xbb
	s_mov_b32 s21, 0xa800
	s_mov_b32 s22, 0x41000000
	s_mov_b32 s23, 0x41000000
	s_cmp_eq_u32 s16, 0
	s_cselect_b32 s20, 0x7, s20
	s_cselect_b32 s21, 0x1c00, s21
	s_cselect_b32 s22, 0x41800000, s22
	s_cselect_b32 s23, 0x41800000, s23
	s_cmp_eq_u32 s16, 22
	s_cselect_b32 s22, 0, s22
	s_cselect_b32 s23, 0, s23
	s_lshl_b32 s20, s20, 9
	v_mad_u32_u24 v6, v3, s21, v4
	v_add_u32_e32 v6, s20, v6
	v_mov_b32_e32 v39, s22
	v_mov_b32_e32 v8, s23
	global_load_dword v23, v6, s[8:9]
	v_cndmask_b32_e32 v39, v39, v8, vcc
	s_lshl2_add_u32 s20, s17, 0x16
	s_mov_b32 s21, 0xa800
	s_mov_b32 s22, 0x41800000
	s_mov_b32 s23, 0x41800000
	s_cmp_eq_u32 s16, 0
	s_cselect_b32 s20, 0x8, s20
	s_cselect_b32 s21, 0x1c00, s21
	s_cmp_eq_u32 s16, 22
	s_cselect_b32 s22, 0, s22
	s_cselect_b32 s23, 0, s23
	s_lshl_b32 s20, s20, 9
	v_mad_u32_u24 v6, v3, s21, v4
	v_add_u32_e32 v6, s20, v6
	v_mov_b32_e32 v40, s22
	v_mov_b32_e32 v8, s23
	global_load_dword v24, v6, s[8:9]
	v_cndmask_b32_e32 v40, v40, v8, vcc
	s_lshl2_add_u32 s20, s17, 0xb8
	s_mov_b32 s21, 0xa800
	s_mov_b32 s22, 0x41000000
	s_mov_b32 s23, 0x41000000
	s_cmp_eq_u32 s16, 0
	s_cselect_b32 s20, 0x9, s20
	s_cselect_b32 s21, 0x1c00, s21
	s_cselect_b32 s22, 0x41800000, s22
	s_cselect_b32 s23, 0x41800000, s23
	s_cmp_eq_u32 s16, 22
	s_cselect_b32 s22, 0, s22
	s_cselect_b32 s23, 0, s23
	s_lshl_b32 s20, s20, 9
	v_mad_u32_u24 v6, v3, s21, v4
	v_add_u32_e32 v6, s20, v6
	v_mov_b32_e32 v41, s22
	v_mov_b32_e32 v8, s23
	global_load_dword v25, v6, s[8:9]
	v_cndmask_b32_e32 v41, v41, v8, vcc
	s_lshl2_add_u32 s20, s17, 0x17
	s_mov_b32 s21, 0xa800
	s_mov_b32 s22, 0x41800000
	s_mov_b32 s23, 0x41800000
	s_cmp_eq_u32 s16, 0
	s_cselect_b32 s20, 0xa, s20
	s_cselect_b32 s21, 0x1c00, s21
	s_cmp_eq_u32 s16, 22
	s_cselect_b32 s22, 0, s22
	s_cselect_b32 s23, 0, s23
	s_lshl_b32 s20, s20, 9
	v_mad_u32_u24 v6, v3, s21, v4
	v_add_u32_e32 v6, s20, v6
	v_mov_b32_e32 v42, s22
	v_mov_b32_e32 v8, s23
	global_load_dword v26, v6, s[8:9]
	v_cndmask_b32_e32 v42, v42, v8, vcc
	s_lshl2_add_u32 s20, s17, 0xb9
	s_mov_b32 s21, 0xa800
	s_mov_b32 s22, 0x41000000
	s_mov_b32 s23, 0x41000000
	s_cmp_eq_u32 s16, 0
	s_cselect_b32 s20, 0xb, s20
	s_cselect_b32 s21, 0x1c00, s21
	s_cselect_b32 s22, 0x41800000, s22
	s_cselect_b32 s23, 0x41800000, s23
	s_cmp_eq_u32 s16, 22
	s_cselect_b32 s22, 0, s22
	s_cselect_b32 s23, 0, s23
	s_lshl_b32 s20, s20, 9
	v_mad_u32_u24 v6, v3, s21, v4
	v_add_u32_e32 v6, s20, v6
	v_mov_b32_e32 v43, s22
	v_mov_b32_e32 v8, s23
	global_load_dword v27, v6, s[8:9]
	v_cndmask_b32_e32 v43, v43, v8, vcc
	s_lshl2_add_u32 s20, s17, 0x18
	s_mov_b32 s21, 0xa800
	s_mov_b32 s22, 0x41800000
	s_mov_b32 s23, 0x41800000
	s_cmp_eq_u32 s16, 0
	s_cselect_b32 s20, 0xc, s20
	s_cselect_b32 s21, 0x1c00, s21
	s_cmp_eq_u32 s16, 20
	s_cselect_b32 s20, 0x6f, s20
	s_cselect_b32 s21, 0x14400, s21
	s_cselect_b32 s23, 0x41000000, s23
	s_cmp_eq_u32 s16, 22
	s_cselect_b32 s22, 0, s22
	s_cselect_b32 s23, 0, s23
	s_lshl_b32 s20, s20, 9
	v_mad_u32_u24 v6, v3, s21, v4
	v_add_u32_e32 v6, s20, v6
	v_mov_b32_e32 v44, s22
	v_mov_b32_e32 v8, s23
	global_load_dword v28, v6, s[8:9]
	v_cndmask_b32_e32 v44, v44, v8, vcc
	s_lshl2_add_u32 s20, s17, 0xba
	s_mov_b32 s21, 0xa800
	s_mov_b32 s22, 0x41000000
	s_mov_b32 s23, 0x41000000
	s_cmp_eq_u32 s16, 0
	s_cselect_b32 s20, 0x6c, s20
	s_cselect_b32 s21, 0x14400, s21
	s_cselect_b32 s22, 0x41800000, s22
	s_cmp_eq_u32 s16, 20
	s_cselect_b32 s20, 0x70, s20
	s_cselect_b32 s21, 0x14400, s21
	s_cselect_b32 s22, 0x41800000, s22
	s_cmp_eq_u32 s16, 22
	s_cselect_b32 s22, 0, s22
	s_cselect_b32 s23, 0, s23
	s_lshl_b32 s20, s20, 9
	v_mad_u32_u24 v6, v3, s21, v4
	v_add_u32_e32 v6, s20, v6
	v_mov_b32_e32 v45, s22
	v_mov_b32_e32 v8, s23
	global_load_dword v29, v6, s[8:9]
	v_cndmask_b32_e32 v45, v45, v8, vcc
	s_lshl2_add_u32 s20, s17, 0x19
	s_mov_b32 s21, 0xa800
	s_mov_b32 s22, 0x41800000
	s_mov_b32 s23, 0x41800000
	s_cmp_eq_u32 s16, 0
	s_cselect_b32 s20, 0x6d, s20
	s_cselect_b32 s21, 0x14400, s21
	s_cselect_b32 s23, 0x41000000, s23
	s_cmp_eq_u32 s16, 20
	s_cselect_b32 s20, 0x71, s20
	s_cselect_b32 s21, 0x14400, s21
	s_cselect_b32 s23, 0x41000000, s23
	s_cmp_eq_u32 s16, 22
	s_cselect_b32 s22, 0, s22
	s_cselect_b32 s23, 0, s23
	s_lshl_b32 s20, s20, 9
	v_mad_u32_u24 v6, v3, s21, v4
	v_add_u32_e32 v6, s20, v6
	v_mov_b32_e32 v46, s22
	v_mov_b32_e32 v8, s23
	global_load_dword v30, v6, s[8:9]
	v_cndmask_b32_e32 v46, v46, v8, vcc
	s_lshl2_add_u32 s20, s17, 0xbb
	s_mov_b32 s21, 0xa800
	s_mov_b32 s22, 0x41000000
	s_mov_b32 s23, 0x41000000
	s_cmp_eq_u32 s16, 0
	s_cselect_b32 s20, 0x6e, s20
	s_cselect_b32 s21, 0x14400, s21
	s_cselect_b32 s22, 0x41800000, s22
	s_cmp_eq_u32 s16, 20
	s_cselect_b32 s20, 0xd, s20
	s_cselect_b32 s21, 0x0, s21
	s_cselect_b32 s22, 0x41800000, s22
	s_cselect_b32 s23, 0x0, s23
	s_cmp_eq_u32 s16, 22
	s_cselect_b32 s22, 0, s22
	s_cselect_b32 s23, 0, s23
	s_lshl_b32 s20, s20, 9
	v_mad_u32_u24 v6, v3, s21, v4
	v_add_u32_e32 v6, s20, v6
	v_mov_b32_e32 v47, s22
	v_mov_b32_e32 v8, s23
	global_load_dword v31, v6, s[8:9]
	v_cndmask_b32_e32 v47, v47, v8, vcc
	s_waitcnt vmcnt(15)
	v_mul_f32_e32 v16, v16, v32
	s_waitcnt vmcnt(14)
	v_mul_f32_e32 v17, v17, v33
	s_waitcnt vmcnt(13)
	v_mul_f32_e32 v18, v18, v34
	s_waitcnt vmcnt(12)
	v_mul_f32_e32 v19, v19, v35
	s_waitcnt vmcnt(11)
	v_mul_f32_e32 v20, v20, v36
	s_waitcnt vmcnt(10)
	v_mul_f32_e32 v21, v21, v37
	s_waitcnt vmcnt(9)
	v_mul_f32_e32 v22, v22, v38
	s_waitcnt vmcnt(8)
	v_mul_f32_e32 v23, v23, v39
	s_waitcnt vmcnt(7)
	v_mul_f32_e32 v24, v24, v40
	s_waitcnt vmcnt(6)
	v_mul_f32_e32 v25, v25, v41
	s_waitcnt vmcnt(5)
	v_mul_f32_e32 v26, v26, v42
	s_waitcnt vmcnt(4)
	v_mul_f32_e32 v27, v27, v43
	s_waitcnt vmcnt(3)
	v_mul_f32_e32 v28, v28, v44
	s_waitcnt vmcnt(2)
	v_mul_f32_e32 v29, v29, v45
	s_waitcnt vmcnt(1)
	v_mul_f32_e32 v30, v30, v46
	s_waitcnt vmcnt(0)
	v_mul_f32_e32 v31, v31, v47
	v_cvt_pk_fp8_f32 v0, v16, v17
	v_cvt_pk_fp8_f32 v1, v20, v21
	v_cvt_pk_fp8_f32 v2, v24, v25
	v_cvt_pk_fp8_f32 v3, v28, v29
	v_cvt_pk_fp8_f32 v0, v18, v19 op_sel:[0,0,1]
	v_cvt_pk_fp8_f32 v1, v22, v23 op_sel:[0,0,1]
	v_cvt_pk_fp8_f32 v2, v26, v27 op_sel:[0,0,1]
	v_cvt_pk_fp8_f32 v3, v30, v31 op_sel:[0,0,1]
	s_nop 1
	global_store_dwordx4 v5, v[0:3], s[6:7]
	s_endpgm

	.amdhsa_kernel _Z11prep_kernelPKfS0_S0_S0_S0_S0_S0_S0_PhPf
		.amdhsa_group_segment_fixed_size 1280
		.amdhsa_private_segment_fixed_size 0
		.amdhsa_kernarg_size 80
		.amdhsa_user_sgpr_count 2
		.amdhsa_user_sgpr_dispatch_ptr 0
		.amdhsa_user_sgpr_queue_ptr 0
		.amdhsa_user_sgpr_kernarg_segment_ptr 1
		.amdhsa_user_sgpr_dispatch_id 0
		.amdhsa_user_sgpr_kernarg_preload_length 0
		.amdhsa_user_sgpr_kernarg_preload_offset 0
		.amdhsa_user_sgpr_private_segment_size 0
		.amdhsa_uses_dynamic_stack 0
		.amdhsa_enable_private_segment 0
		.amdhsa_system_sgpr_workgroup_id_x 1
		.amdhsa_system_sgpr_workgroup_id_y 0
		.amdhsa_system_sgpr_workgroup_id_z 0
		.amdhsa_system_sgpr_workgroup_info 0
		.amdhsa_system_vgpr_workitem_id 0
		.amdhsa_next_free_vgpr 63
		.amdhsa_next_free_sgpr 24
		.amdhsa_accum_offset 64
		.amdhsa_reserve_vcc 1
		.amdhsa_float_round_mode_32 0
		.amdhsa_float_round_mode_16_64 0
		.amdhsa_float_denorm_mode_32 3
		.amdhsa_float_denorm_mode_16_64 3
		.amdhsa_dx10_clamp 1
		.amdhsa_ieee_mode 1
		.amdhsa_fp16_overflow 0
		.amdhsa_tg_split 0
		.amdhsa_exception_fp_ieee_invalid_op 0
		.amdhsa_exception_fp_denorm_src 0
		.amdhsa_exception_fp_ieee_div_zero 0
		.amdhsa_exception_fp_ieee_overflow 0
		.amdhsa_exception_fp_ieee_underflow 0
		.amdhsa_exception_fp_ieee_inexact 0
		.amdhsa_exception_int_div_zero 0
	.end_amdhsa_kernel

amdhsa.kernels:
  - .agpr_count:     0
    .args:
      - .actual_access:  read_only
        .address_space:  global
        .offset:         0
        .size:           8
        .value_kind:     global_buffer
      - .actual_access:  read_only
        .address_space:  global
        .offset:         8
        .size:           8
        .value_kind:     global_buffer
      - .actual_access:  read_only
        .address_space:  global
        .offset:         16
        .size:           8
        .value_kind:     global_buffer
      - .actual_access:  read_only
        .address_space:  global
        .offset:         24
        .size:           8
        .value_kind:     global_buffer
      - .actual_access:  read_only
        .address_space:  global
        .offset:         32
        .size:           8
        .value_kind:     global_buffer
      - .actual_access:  read_only
        .address_space:  global
        .offset:         40
        .size:           8
        .value_kind:     global_buffer
      - .actual_access:  read_only
        .address_space:  global
        .offset:         48
        .size:           8
        .value_kind:     global_buffer
      - .actual_access:  read_only
        .address_space:  global
        .offset:         56
        .size:           8
        .value_kind:     global_buffer
      - .actual_access:  write_only
        .address_space:  global
        .offset:         64
        .size:           8
        .value_kind:     global_buffer
      - .actual_access:  write_only
        .address_space:  global
        .offset:         72
        .size:           8
        .value_kind:     global_buffer
    .group_segment_fixed_size: 1280
    .kernarg_segment_align: 8
    .kernarg_segment_size: 80
    .language:       OpenCL C
    .language_version:
      - 2
      - 0
    .max_flat_workgroup_size: 256
    .name:           _Z11prep_kernelPKfS0_S0_S0_S0_S0_S0_S0_PhPf
    .private_segment_fixed_size: 0
    .sgpr_count:     30
    .sgpr_spill_count: 0
    .symbol:         _Z11prep_kernelPKfS0_S0_S0_S0_S0_S0_S0_PhPf.kd
    .uniform_work_group_size: 1
    .uses_dynamic_stack: false
    .vgpr_count:     63
    .vgpr_spill_count: 0
    .wavefront_size: 64
  - .agpr_count:     0
    .args:
      - .actual_access:  read_only
        .address_space:  global
        .offset:         0
        .size:           8
        .value_kind:     global_buffer
      - .address_space:  global
        .offset:         8
        .size:           8
        .value_kind:     global_buffer
      - .actual_access:  read_only
        .address_space:  global
        .offset:         16
        .size:           8
        .value_kind:     global_buffer
      - .actual_access:  read_only
        .address_space:  global
        .offset:         24
        .size:           8
        .value_kind:     global_buffer
      - .actual_access:  write_only
        .address_space:  global
        .offset:         32
        .size:           8
        .value_kind:     global_buffer
    .group_segment_fixed_size: 0
    .kernarg_segment_align: 8
    .kernarg_segment_size: 40
    .language:       OpenCL C
    .language_version:
      - 2
      - 0
    .max_flat_workgroup_size: 512
    .name:           _Z13render_kernelPKfPKhS0_S0_Pf
    .private_segment_fixed_size: 0
    .sgpr_count:     28
    .sgpr_spill_count: 0
    .symbol:         _Z13render_kernelPKfPKhS0_S0_Pf.kd
    .uniform_work_group_size: 1
    .uses_dynamic_stack: false
    .vgpr_count:     256
    .vgpr_spill_count: 0
    .wavefront_size: 64
